# grid barrier: agent-scope L1 invalidate issued at arrival (all waves parked, only sc1 polls in flight) instead of after the release poll; leader issues it together with the L2 write-back
# speedup vs baseline: 1.0252x; 1.0156x over previous
.LBB0_166:
	s_or_b64 exec, exec, s[4:5]
	v_readlane_b32 s4, v245, 24
	v_readlane_b32 s5, v245, 25
	s_waitcnt vmcnt(0)
	s_nop 2
	s_waitcnt vmcnt(0)

.LBB0_240:
	v_readlane_b32 s4, v245, 22
	v_readlane_b32 s5, v245, 23
	v_cvt_f32_u32_e32 v1, v3
	v_sub_u32_e32 v5, 0, v3
	v_rcp_iflag_f32_e32 v1, v1
	s_nop 1
	global_atomic_add v4, v195, v203, s[4:5] sc0
	v_mul_f32_e32 v1, 0x4f7ffffe, v1
	v_cvt_u32_f32_e32 v1, v1
	v_mul_lo_u32 v5, v5, v1
	v_mul_hi_u32 v5, v1, v5
	v_add_u32_e32 v1, v1, v5
	s_waitcnt vmcnt(0)
	v_mul_hi_u32 v1, v4, v1
	v_mul_lo_u32 v5, v1, v3
	v_sub_u32_e32 v5, v4, v5
	v_add_u32_e32 v6, 1, v1
	v_cmp_ge_u32_e32 vcc, v5, v3
	v_add_u32_e32 v4, 1, v4
	s_nop 0
	v_cndmask_b32_e32 v1, v1, v6, vcc
	v_sub_u32_e32 v6, v5, v3
	v_cndmask_b32_e32 v5, v5, v6, vcc
	v_add_u32_e32 v6, 1, v1
	v_cmp_ge_u32_e32 vcc, v5, v3
	s_nop 1
	v_cndmask_b32_e32 v1, v1, v6, vcc
	v_mul_lo_u32 v5, v3, v1
	v_add_u32_e32 v3, v5, v3
	v_cmp_ne_u32_e32 vcc, v4, v3
	s_and_saveexec_b64 s[4:5], vcc
	s_xor_b64 s[4:5], exec, s[4:5]
	s_cbranch_execz .LBB0_254
	buffer_inv sc1
	v_readlane_b32 s6, v245, 24
	v_readlane_b32 s7, v245, 25
	s_waitcnt lgkmcnt(0)
	s_nop 3
	global_load_dword v2, v195, s[6:7] sc1
	s_waitcnt vmcnt(0)
	v_cmp_eq_u32_e32 vcc, v2, v1
	s_and_saveexec_b64 s[6:7], vcc
	s_cbranch_execz .LBB0_253
	s_mov_b32 s19, 1
	s_mov_b64 s[8:9], 0
	s_branch .LBB0_244

.LBB0_253:
	s_or_b64 exec, exec, s[6:7]
	s_waitcnt vmcnt(0)
	s_waitcnt vmcnt(0)
.LBB0_254:
	s_andn2_saveexec_b64 s[4:5], s[4:5]
	s_cbranch_execz .LBB0_272
	s_mov_b64 s[4:5], exec
	buffer_wbl2 sc1
	buffer_inv sc1
	s_waitcnt lgkmcnt(0)
	s_waitcnt vmcnt(0)
	v_mbcnt_lo_u32_b32 v1, s4, 0
	v_mbcnt_hi_u32_b32 v1, s5, v1
	v_cmp_eq_u32_e32 vcc, 0, v1
	s_and_saveexec_b64 s[6:7], vcc
	s_cbranch_execz .LBB0_257
	s_bcnt1_i32_b64 s4, s[4:5]
	v_mov_b32_e32 v3, s4
	v_readlane_b32 s4, v245, 26
	v_readlane_b32 s5, v245, 27
	s_nop 4
	global_atomic_add v3, v195, v3, s[4:5] sc0

.LBB0_518:
	v_readlane_b32 s4, v245, 22
	v_readlane_b32 s5, v245, 23
	v_cvt_f32_u32_e32 v1, v3
	v_sub_u32_e32 v5, 0, v3
	v_rcp_iflag_f32_e32 v1, v1
	s_nop 1
	global_atomic_add v4, v195, v203, s[4:5] sc0
	v_mul_f32_e32 v1, 0x4f7ffffe, v1
	v_cvt_u32_f32_e32 v1, v1
	v_mul_lo_u32 v5, v5, v1
	v_mul_hi_u32 v5, v1, v5
	v_add_u32_e32 v1, v1, v5
	s_waitcnt vmcnt(0)
	v_mul_hi_u32 v1, v4, v1
	v_mul_lo_u32 v5, v1, v3
	v_sub_u32_e32 v5, v4, v5
	v_add_u32_e32 v6, 1, v1
	v_cmp_ge_u32_e32 vcc, v5, v3
	v_add_u32_e32 v4, 1, v4
	s_nop 0
	v_cndmask_b32_e32 v1, v1, v6, vcc
	v_sub_u32_e32 v6, v5, v3
	v_cndmask_b32_e32 v5, v5, v6, vcc
	v_add_u32_e32 v6, 1, v1
	v_cmp_ge_u32_e32 vcc, v5, v3
	s_nop 1
	v_cndmask_b32_e32 v1, v1, v6, vcc
	v_mul_lo_u32 v5, v3, v1
	v_add_u32_e32 v3, v5, v3
	v_cmp_ne_u32_e32 vcc, v4, v3
	s_and_saveexec_b64 s[4:5], vcc
	s_xor_b64 s[4:5], exec, s[4:5]
	s_cbranch_execz .LBB0_532
	buffer_inv sc1
	v_readlane_b32 s6, v245, 24
	v_readlane_b32 s7, v245, 25
	s_waitcnt lgkmcnt(0)
	s_nop 3
	global_load_dword v2, v195, s[6:7] sc1
	s_waitcnt vmcnt(0)
	v_cmp_eq_u32_e32 vcc, v2, v1
	s_and_saveexec_b64 s[6:7], vcc
	s_cbranch_execz .LBB0_531
	s_mov_b32 s18, 1
	s_mov_b64 s[8:9], 0
	s_branch .LBB0_522

.LBB0_877:
	s_mov_b64 s[4:5], exec
	buffer_wbl2 sc1
	buffer_inv sc1
	s_waitcnt lgkmcnt(0)
	s_waitcnt vmcnt(0)
	v_mbcnt_lo_u32_b32 v1, s4, 0
	v_mbcnt_hi_u32_b32 v1, s5, v1
	v_cmp_eq_u32_e32 vcc, 0, v1
	s_and_saveexec_b64 s[6:7], vcc
	s_cbranch_execz .LBB0_879
	s_bcnt1_i32_b64 s4, s[4:5]
	v_mov_b32_e32 v3, s4
	v_readlane_b32 s4, v245, 26
	v_readlane_b32 s5, v245, 27
	s_nop 4
	global_atomic_add v3, v195, v3, s[4:5] sc0
